# MoE phases use only the workgroups the round count needs (rest convert weights all phase); mixer MFMA blocks with batched LDS reads; mixer next-chunk LDS-DMA issued earlier
# speedup vs baseline: 1.0144x; 1.0144x over previous
.LBB0_465:
	s_waitcnt lgkmcnt(0)
	s_barrier
	ds_read_b128 v[10:13], v127
	ds_read_b128 v[14:17], v127 offset:64
	ds_read_b128 v[56:59], v127 offset:128
	ds_read_b128 v[60:63], v127 offset:192
	ds_read_b128 v[64:67], v128 offset:17408
	ds_read_b128 v[68:71], v128 offset:17472
	ds_read_b128 v[72:75], v128 offset:17536
	ds_read_b128 v[76:79], v128 offset:17600
	ds_read_b128 v[176:179], v128 offset:21760
	ds_read_b128 v[180:183], v128 offset:21824
	ds_read_b128 v[184:187], v128 offset:21888
	ds_read_b128 v[188:191], v128 offset:21952
	s_waitcnt lgkmcnt(7)
	v_mfma_f32_16x16x32_bf16 v[2:5], v[64:67], v[10:13], 0
	s_waitcnt lgkmcnt(6)
	v_mfma_f32_16x16x32_bf16 v[2:5], v[68:71], v[14:17], v[2:5]
	s_waitcnt lgkmcnt(3)
	v_mfma_f32_16x16x32_bf16 v[6:9], v[176:179], v[10:13], 0
	v_mfma_f32_16x16x32_bf16 v[2:5], v[72:75], v[56:59], v[2:5]
	s_waitcnt lgkmcnt(2)
	v_mfma_f32_16x16x32_bf16 v[6:9], v[180:183], v[14:17], v[6:9]
	v_mfma_f32_16x16x32_bf16 v[2:5], v[76:79], v[60:63], v[2:5]
	s_waitcnt lgkmcnt(1)
	v_mfma_f32_16x16x32_bf16 v[6:9], v[184:187], v[56:59], v[6:9]
	s_waitcnt lgkmcnt(0)
	v_mfma_f32_16x16x32_bf16 v[6:9], v[188:191], v[60:63], v[6:9]
	s_nop 6
	v_cndmask_b32_e64 v56, v2, 0, s[44:45]
	v_cndmask_b32_e64 v57, 0, v3, s[46:47]
	v_cndmask_b32_e64 v58, v4, 0, s[48:49]
	v_cndmask_b32_e64 v59, v5, 0, s[50:51]
	v_cvt_pk_bf16_f32 v56, v56, v57
	v_cvt_pk_bf16_f32 v57, v58, v59
	ds_write_b64 v129, v[56:57]
	v_cndmask_b32_e64 v6, v6, 0, s[52:53]
	v_cndmask_b32_e64 v7, 0, v7, s[54:55]
	v_cndmask_b32_e64 v8, v8, 0, s[56:57]
	v_cndmask_b32_e64 v9, v9, 0, s[58:59]
	v_cvt_pk_bf16_f32 v6, v6, v7
	v_cvt_pk_bf16_f32 v7, v8, v9
	ds_write_b64 v130, v[6:7]
	s_waitcnt lgkmcnt(0)
	s_barrier
	ds_read_b128 v[10:13], v131
	ds_read_b128 v[14:17], v132
	ds_read_b128 v[56:59], v133
	ds_read_b128 v[60:63], v131 offset:64
	ds_read_b128 v[64:67], v132 offset:64
	ds_read_b128 v[68:71], v133 offset:64
	ds_read_b128 v[72:75], v138
	ds_read_b128 v[76:79], v134 offset:52224
	ds_read_b128 v[176:179], v137
	ds_read_b128 v[180:183], v137 offset:2304
	ds_read_b128 v[184:187], v137 offset:4608
	ds_read_b128 v[188:191], v137 offset:6912
	ds_read_b128 v[200:203], v134 offset:52288
	ds_read_b128 v[204:207], v137 offset:64
	ds_read_b128 v[208:211], v137 offset:2368
	s_waitcnt lgkmcnt(13)
	v_mfma_f32_16x16x32_bf16 v[6:9], v[10:13], v[14:17], 0
	s_waitcnt lgkmcnt(12)
	v_mfma_f32_16x16x32_bf16 v[2:5], v[10:13], v[56:59], 0
	ds_read_b128 v[212:215], v137 offset:4672
	ds_read_b128 v[220:223], v137 offset:6976
	ds_read_b128 v[224:227], v135
	s_waitcnt lgkmcnt(13)
	v_mfma_f32_16x16x32_bf16 v[6:9], v[60:63], v[64:67], v[6:9]
	s_waitcnt lgkmcnt(12)
	v_mfma_f32_16x16x32_bf16 v[2:5], v[60:63], v[68:71], v[2:5]
	ds_read_b128 v[232:235], v128
	ds_read_b128 v[236:239], v136
	ds_read_b128 v[14:17], v135 offset:64
	s_waitcnt lgkmcnt(14)
	v_pk_mul_f32 v[22:23], v[22:23], v[72:73]
	v_pk_mul_f32 v[24:25], v[24:25], v[74:75]
	v_pk_mul_f32 v[26:27], v[26:27], v[72:73]
	v_pk_mul_f32 v[28:29], v[28:29], v[74:75]
	v_pk_mul_f32 v[30:31], v[30:31], v[72:73]
	v_pk_mul_f32 v[32:33], v[32:33], v[74:75]
	v_pk_mul_f32 v[34:35], v[34:35], v[72:73]
	v_pk_mul_f32 v[36:37], v[36:37], v[74:75]
	s_waitcnt lgkmcnt(12)
	v_mfma_f32_16x16x32_bf16 v[22:25], v[76:79], v[176:179], v[22:25]
	s_waitcnt lgkmcnt(11)
	v_mfma_f32_16x16x32_bf16 v[26:29], v[76:79], v[180:183], v[26:29]
	s_waitcnt lgkmcnt(10)
	v_mfma_f32_16x16x32_bf16 v[30:33], v[76:79], v[184:187], v[30:33]
	s_waitcnt lgkmcnt(9)
	v_mfma_f32_16x16x32_bf16 v[34:37], v[76:79], v[188:191], v[34:37]
	ds_read_b128 v[10:13], v128 offset:64
	ds_read_b128 v[56:59], v136 offset:64
	ds_read_b128 v[64:67], v135 offset:128
	ds_read_b128 v[60:63], v128 offset:128
	s_waitcnt lgkmcnt(11)
	v_mfma_f32_16x16x32_bf16 v[22:25], v[200:203], v[204:207], v[22:25]
	s_waitcnt lgkmcnt(10)
	v_mfma_f32_16x16x32_bf16 v[26:29], v[200:203], v[208:211], v[26:29]
	ds_read_b128 v[68:71], v136 offset:128
	ds_read_b128 v[72:75], v135 offset:192
	s_waitcnt lgkmcnt(11)
	v_mfma_f32_16x16x32_bf16 v[30:33], v[200:203], v[212:215], v[30:33]
	s_waitcnt lgkmcnt(10)
	v_mfma_f32_16x16x32_bf16 v[34:37], v[200:203], v[220:223], v[34:37]
	ds_read_b128 v[176:179], v128 offset:192
	ds_read_b128 v[180:183], v136 offset:192
	s_waitcnt lgkmcnt(10)
	v_mfma_f32_16x16x32_bf16 v[6:9], v[224:227], v[232:235], v[6:9]
	s_waitcnt lgkmcnt(9)
	v_mfma_f32_16x16x32_bf16 v[2:5], v[224:227], v[236:239], v[2:5]
	s_waitcnt lgkmcnt(7)
	v_mfma_f32_16x16x32_bf16 v[6:9], v[14:17], v[10:13], v[6:9]
	s_waitcnt lgkmcnt(6)
	v_mfma_f32_16x16x32_bf16 v[2:5], v[14:17], v[56:59], v[2:5]
	s_waitcnt lgkmcnt(4)
	v_mfma_f32_16x16x32_bf16 v[6:9], v[64:67], v[60:63], v[6:9]
	s_waitcnt lgkmcnt(3)
	v_mfma_f32_16x16x32_bf16 v[2:5], v[64:67], v[68:71], v[2:5]
	s_waitcnt lgkmcnt(1)
	v_mfma_f32_16x16x32_bf16 v[6:9], v[72:75], v[176:179], v[6:9]
	s_waitcnt lgkmcnt(0)
	v_mfma_f32_16x16x32_bf16 v[2:5], v[72:75], v[180:183], v[2:5]
	v_add_u32_e32 v57, s24, v118
	v_add_u32_e32 v56, s4, v109
	v_add_u32_e32 v58, 0x7ff, v57
	s_add_i32 s4, s4, 64
	s_sub_i32 s24, s24, 64
	v_cndmask_b32_e64 v58, v58, v56, s[76:77]
	s_cmpk_eq_i32 s4, 0x800
	s_waitcnt vmcnt(0)
	s_nop 0
	v_cvt_pk_bf16_f32 v6, v6, v7
	v_cvt_pk_bf16_f32 v7, v8, v9
	v_or_b32_e32 v8, s84, v58
	v_ashrrev_i32_e32 v9, 31, v8
	v_lshl_add_u64 v[8:9], v[8:9], 0, s[2:3]
	v_mad_u64_u32 v[14:15], s[8:9], v8, s11, v[54:55]
	v_mad_i32_i24 v15, v9, s11, v15
	global_store_dwordx2 v[14:15], v[6:7], off
	v_add_u32_e32 v6, 16, v56
	v_add_u32_e32 v7, 0x7ef, v57
	v_cndmask_b32_e64 v6, v7, v6, s[76:77]
	v_cvt_pk_bf16_f32 v2, v2, v3
	v_cvt_pk_bf16_f32 v3, v4, v5
	v_or_b32_e32 v4, s84, v6
	v_ashrrev_i32_e32 v5, 31, v4
	v_lshl_add_u64 v[4:5], v[4:5], 0, s[2:3]
	v_mad_u64_u32 v[6:7], s[8:9], v4, s11, v[54:55]
	v_mad_i32_i24 v7, v5, s11, v7
	global_store_dwordx2 v[6:7], v[2:3], off
	s_cbranch_scc1 .LBB0_448
.LBB0_466:
	v_cndmask_b32_e64 v2, 0, 1, s[38:39]
	v_cmp_ne_u32_e64 s[78:79], 1, v2
	s_andn2_b64 vcc, exec, s[38:39]
	s_mov_b64 s[8:9], -1
	s_cbranch_vccnz .LBB0_468
	v_add_u32_e32 v8, s94, v106
	ds_read2st64_b32 v[2:3], v8 offset1:1
	v_add_u32_e32 v16, s94, v105
	ds_read2st64_b32 v[4:5], v8 offset0:2 offset1:3
	ds_read2st64_b32 v[6:7], v8 offset0:4 offset1:5
	ds_read2st64_b32 v[8:9], v8 offset0:6 offset1:7
	s_mov_b64 s[8:9], 0
	s_waitcnt lgkmcnt(0)
	v_lshlrev_b32_e32 v60, 16, v4
	v_lshlrev_b32_e32 v10, 16, v2
	v_mul_f32_e32 v10, 0xbfb8aa3b, v10
	v_exp_f32_e32 v12, v10
	v_and_b32_e32 v2, 0xffff0000, v2
	ds_read2st64_b32 v[10:11], v16 offset1:1
	v_mul_f32_e32 v2, 0xbfb8aa3b, v2
	v_add_f32_e32 v12, 1.0, v12
	v_rcp_f32_e32 v58, v12
	v_exp_f32_e32 v2, v2
	s_waitcnt lgkmcnt(0)
	v_lshlrev_b32_e32 v56, 16, v10
	v_and_b32_e32 v57, 0xffff0000, v10
	v_fma_f32 v10, v45, v58, v140
	v_lshlrev_b32_e32 v58, 16, v3
	v_and_b32_e32 v3, 0xffff0000, v3
	v_add_f32_e32 v2, 1.0, v2
	v_mul_f32_e32 v3, 0xbfb8aa3b, v3
	v_rcp_f32_e32 v2, v2
	v_exp_f32_e32 v3, v3
	v_and_b32_e32 v4, 0xffff0000, v4
	v_mul_f32_e32 v4, 0xbfb8aa3b, v4
	v_fma_f32 v2, v143, v2, v139
	v_add_f32_e32 v3, 1.0, v3
	v_max_f32_e32 v74, 0x358637bd, v2
	v_mul_f32_e32 v58, 0xbfb8aa3b, v58
	v_rcp_f32_e32 v3, v3
	v_exp_f32_e32 v4, v4
	v_log_f32_e32 v2, v74
	v_exp_f32_e32 v58, v58
	v_lshlrev_b32_e32 v62, 16, v5
	v_and_b32_e32 v5, 0xffff0000, v5
	v_fma_f32 v3, v143, v3, v139
	v_add_f32_e32 v4, 1.0, v4
	v_mul_f32_e32 v5, 0xbfb8aa3b, v5
	v_add_f32_e32 v88, 0, v2
	v_add_f32_e32 v2, 1.0, v58
	v_lshlrev_b32_e32 v58, 16, v11
	v_and_b32_e32 v59, 0xffff0000, v11
	v_max_f32_e32 v11, 0x358637bd, v3
	v_mul_f32_e32 v60, 0xbfb8aa3b, v60
	v_rcp_f32_e32 v4, v4
	v_exp_f32_e32 v5, v5
	v_log_f32_e32 v3, v11
	v_exp_f32_e32 v60, v60
	ds_read2st64_b32 v[12:13], v16 offset0:2 offset1:3
	ds_read2st64_b32 v[14:15], v16 offset0:4 offset1:5
	ds_read2st64_b32 v[16:17], v16 offset0:6 offset1:7
	v_lshlrev_b32_e32 v64, 16, v6
	v_and_b32_e32 v6, 0xffff0000, v6
	v_fma_f32 v4, v143, v4, v139
	v_add_f32_e32 v5, 1.0, v5
	v_mul_f32_e32 v6, 0xbfb8aa3b, v6
	v_add_f32_e32 v86, v88, v3
	v_add_f32_e32 v3, 1.0, v60
	s_waitcnt lgkmcnt(0)
	s_cmpk_eq_i32 s4, 0x7c0
	s_cbranch_scc1 .Lmx_qk_skip_h
	v_add_u32_e32 v176, s4, v110
	v_add_u32_e32 v177, s24, v121
	v_add_u32_e32 v178, 64, v176
	v_add_u32_e32 v179, 0x7bf, v177
	v_cndmask_b32_e64 v178, v179, v178, s[76:77]
	v_add_u32_e32 v178, s84, v178
	v_mad_i64_i32 v[178:179], s[100:101], v178, s20, v[38:39]
	s_mov_b32 m0, s19
	v_lshl_add_u64 v[180:181], v[178:179], 0, s[80:81]
	global_load_lds_dwordx4 v[180:181], off
	v_lshl_add_u64 v[178:179], v[178:179], 0, s[6:7]
	s_mov_b32 m0, s82
	v_add_u32_e32 v176, 0x44, v176
	global_load_lds_dwordx4 v[178:179], off
	v_add_u32_e32 v178, 0x7bb, v177
	v_cndmask_b32_e64 v176, v178, v176, s[76:77]
	v_add_u32_e32 v176, s84, v176
	v_mad_i64_i32 v[178:179], s[100:101], v176, s20, v[38:39]
	v_lshl_add_u64 v[180:181], v[178:179], 0, s[80:81]
	s_mov_b32 m0, s85
	v_lshl_add_u64 v[178:179], v[178:179], 0, s[6:7]
	global_load_lds_dwordx4 v[180:181], off
	s_mov_b32 m0, s86
	s_nop 0
	global_load_lds_dwordx4 v[178:179], off
.Lmx_qk_skip_h:
	v_lshlrev_b32_e32 v60, 16, v12
	v_and_b32_e32 v61, 0xffff0000, v12
	v_max_f32_e32 v12, 0x358637bd, v4
	v_mul_f32_e32 v62, 0xbfb8aa3b, v62
	v_rcp_f32_e32 v5, v5
	v_exp_f32_e32 v6, v6
	v_log_f32_e32 v4, v12
	v_exp_f32_e32 v62, v62
	v_lshlrev_b32_e32 v66, 16, v7
	v_and_b32_e32 v7, 0xffff0000, v7
	v_fma_f32 v5, v143, v5, v139
	v_add_f32_e32 v6, 1.0, v6
	v_mul_f32_e32 v7, 0xbfb8aa3b, v7
	v_add_f32_e32 v84, v86, v4
	v_add_f32_e32 v4, 1.0, v62
	v_lshlrev_b32_e32 v62, 16, v13
	v_and_b32_e32 v63, 0xffff0000, v13
	v_max_f32_e32 v13, 0x358637bd, v5
	v_mul_f32_e32 v64, 0xbfb8aa3b, v64
	v_rcp_f32_e32 v6, v6
	v_exp_f32_e32 v7, v7
	v_log_f32_e32 v5, v13
	v_exp_f32_e32 v64, v64
	v_lshlrev_b32_e32 v68, 16, v8
	v_and_b32_e32 v8, 0xffff0000, v8
	v_fma_f32 v6, v143, v6, v139
	v_add_f32_e32 v7, 1.0, v7
	v_mul_f32_e32 v8, 0xbfb8aa3b, v8
	v_add_f32_e32 v82, v84, v5
	v_add_f32_e32 v5, 1.0, v64
	s_waitcnt lgkmcnt(1)
	v_lshlrev_b32_e32 v64, 16, v14
	v_and_b32_e32 v65, 0xffff0000, v14
	v_max_f32_e32 v14, 0x358637bd, v6
	v_mul_f32_e32 v66, 0xbfb8aa3b, v66
	v_rcp_f32_e32 v7, v7
	v_exp_f32_e32 v8, v8
	v_log_f32_e32 v6, v14
	v_exp_f32_e32 v66, v66
	v_fma_f32 v7, v143, v7, v139
	v_add_f32_e32 v8, 1.0, v8
	v_add_f32_e32 v78, v82, v6
	v_add_f32_e32 v6, 1.0, v66
	v_lshlrev_b32_e32 v66, 16, v15
	v_and_b32_e32 v67, 0xffff0000, v15
	v_max_f32_e32 v15, 0x358637bd, v7
	v_mul_f32_e32 v68, 0xbfb8aa3b, v68
	v_rcp_f32_e32 v8, v8
	v_lshlrev_b32_e32 v70, 16, v9
	v_and_b32_e32 v9, 0xffff0000, v9
	v_log_f32_e32 v7, v15
	v_exp_f32_e32 v68, v68
	v_mul_f32_e32 v9, 0xbfb8aa3b, v9
	v_exp_f32_e32 v9, v9
	v_fma_f32 v8, v143, v8, v139
	v_add_f32_e32 v80, v78, v7
	v_add_f32_e32 v7, 1.0, v68
	s_waitcnt lgkmcnt(0)
	v_lshlrev_b32_e32 v68, 16, v16
	v_and_b32_e32 v69, 0xffff0000, v16
	v_max_f32_e32 v16, 0x358637bd, v8
	v_mul_f32_e32 v70, 0xbfb8aa3b, v70
	v_log_f32_e32 v8, v16
	v_exp_f32_e32 v70, v70
	v_add_f32_e32 v9, 1.0, v9
	v_rcp_f32_e32 v9, v9
	v_rcp_f32_e32 v2, v2
	v_rcp_f32_e32 v3, v3
	v_rcp_f32_e32 v4, v4
	v_rcp_f32_e32 v5, v5
	v_rcp_f32_e32 v6, v6
	v_rcp_f32_e32 v7, v7
	v_add_f32_e32 v73, v80, v8
	v_add_f32_e32 v8, 1.0, v70
	v_rcp_f32_e32 v8, v8
	v_fma_f32 v9, v143, v9, v139
	v_max_f32_e32 v10, 0x358637bd, v10
	v_fma_f32 v2, v45, v2, v140
	v_max_f32_e32 v75, 0x358637bd, v9
	v_log_f32_e32 v72, v10
	v_max_f32_e32 v2, 0x358637bd, v2
	v_fma_f32 v3, v45, v3, v140
	v_lshlrev_b32_e32 v70, 16, v17
	v_and_b32_e32 v71, 0xffff0000, v17
	v_sub_f32_e32 v17, 1.0, v75
	v_log_f32_e32 v75, v75
	v_log_f32_e32 v79, v2
	v_max_f32_e32 v3, 0x358637bd, v3
	v_fma_f32 v4, v45, v4, v140
	v_fma_f32 v5, v45, v5, v140
	v_fma_f32 v6, v45, v6, v140
	v_fma_f32 v7, v45, v7, v140
	v_log_f32_e32 v81, v3
	v_max_f32_e32 v4, 0x358637bd, v4
	v_max_f32_e32 v5, 0x358637bd, v5
	v_max_f32_e32 v6, 0x358637bd, v6
	v_max_f32_e32 v7, 0x358637bd, v7
	v_fma_f32 v8, v45, v8, v140
	v_log_f32_e32 v83, v4
	v_log_f32_e32 v85, v5
	v_log_f32_e32 v87, v6
	v_log_f32_e32 v89, v7
	v_max_f32_e32 v76, 0x358637bd, v8
	v_sub_f32_e32 v8, 1.0, v7
	v_sub_f32_e32 v7, 1.0, v6
	v_sub_f32_e32 v6, 1.0, v5
	v_sub_f32_e32 v5, 1.0, v4
	v_sub_f32_e32 v4, 1.0, v3
	v_sub_f32_e32 v3, 1.0, v2
	v_sub_f32_e32 v2, 1.0, v10
	v_sub_f32_e32 v10, 1.0, v74
	v_mov_b32_e32 v74, v195
	v_sub_f32_e32 v9, 1.0, v76
	v_log_f32_e32 v91, v76
	v_pk_add_f32 v[76:77], v[72:73], v[74:75]
	v_sub_f32_e32 v16, 1.0, v16
	v_add_f32_e32 v157, v76, v79
	v_add_f32_e32 v156, v157, v81
	v_add_f32_e32 v155, v156, v83
	v_add_f32_e32 v154, v155, v85
	v_add_f32_e32 v92, v154, v87
	v_add_f32_e32 v90, v92, v89
	v_add_f32_e32 v72, v90, v91
	v_sub_f32_e32 v15, 1.0, v15
	v_sub_f32_e32 v14, 1.0, v14
	v_sub_f32_e32 v13, 1.0, v13
	v_sub_f32_e32 v12, 1.0, v12
	v_sub_f32_e32 v11, 1.0, v11
	v_mov_b32_e32 v158, v76
	v_mov_b32_e32 v76, v72
.LBB0_468:
	s_andn2_b64 vcc, exec, s[8:9]
	s_cbranch_vccnz .LBB0_470
	s_add_i32 s8, s35, s24
	s_add_i32 s5, s95, s4
	s_add_i32 s40, s8, 0x7ff
	s_and_b64 s[8:9], s[76:77], exec
	s_cselect_b32 s5, s5, s40
	v_cvt_f32_i32_e32 v2, s5
	v_add_u32_e32 v10, s83, v105
	v_add_u32_e32 v11, s83, v106
	v_add_u32_e32 v6, s19, v107
	v_mul_f32_e32 v3, v142, v2
	v_mul_f32_e32 v2, v141, v2
	v_mul_f32_e32 v4, 0.15915494, v3
	v_mul_f32_e32 v5, 0.15915494, v2
	v_rndne_f32_e32 v4, v4
	v_fma_f32 v3, v3, 0.15915494, -v4
	v_rndne_f32_e32 v4, v5
	v_fma_f32 v4, v2, 0.15915494, -v4
	v_sin_f32_e32 v2, v3
	v_cos_f32_e32 v8, v3
	v_sin_f32_e32 v3, v4
	v_cos_f32_e32 v9, v4
	v_add_u32_e32 v4, s19, v104
	v_add_u32_e32 v5, s82, v104
	v_add_u32_e32 v7, s82, v107
	v_add_u32_e32 v12, s83, v114
	v_add_u32_e32 v13, s83, v115
	ds_read_b32 v14, v4
	ds_read_b32 v62, v5
	ds_read_b32 v15, v6
	ds_read_b32 v63, v7
	ds_read_b32 v10, v10
	ds_read_b32 v64, v11
	ds_read_b32 v11, v12
	ds_read_b32 v65, v13
	s_waitcnt lgkmcnt(0)
	v_lshlrev_b32_e32 v6, 16, v15
	v_and_b32_e32 v7, 0xffff0000, v15
	v_pk_mul_f32 v[12:13], v[46:47], v[2:3]
	v_lshlrev_b32_e32 v4, 16, v14
	v_and_b32_e32 v5, 0xffff0000, v14
	v_pk_mul_f32 v[6:7], v[12:13], v[6:7]
	v_add_u32_e32 v66, s14, v114
	v_pk_fma_f32 v[56:57], v[8:9], v[4:5], v[6:7]
	s_waitcnt lgkmcnt(3)
	v_lshlrev_b32_e32 v4, 16, v10
	v_and_b32_e32 v5, 0xffff0000, v10
	s_waitcnt lgkmcnt(1)
	v_lshlrev_b32_e32 v6, 16, v11
	v_and_b32_e32 v7, 0xffff0000, v11
	v_pk_mul_f32 v[10:11], v[50:51], v[2:3]
	v_pk_mul_f32 v[2:3], v[48:49], v[2:3]
	v_pk_fma_f32 v[16:17], v[48:49], v[8:9], v[10:11] neg_lo:[0,0,1] neg_hi:[0,0,1]
	v_pk_fma_f32 v[60:61], v[50:51], v[8:9], v[2:3]
	v_mov_b32_e32 v10, v8
	v_pk_mul_f32 v[14:15], v[46:47], v[60:61]
	v_add_u32_e32 v8, s18, v105
	v_pk_mul_f32 v[2:3], v[14:15], v[6:7]
	s_waitcnt lgkmcnt(0)
	v_lshlrev_b32_e32 v7, 16, v65
	v_lshlrev_b32_e32 v6, 16, v62
	v_mov_b32_e32 v11, v14
	v_pk_fma_f32 v[58:59], v[16:17], v[4:5], v[2:3]
	v_lshlrev_b32_e32 v3, 16, v64
	v_lshlrev_b32_e32 v2, 16, v63
	v_pk_mul_f32 v[6:7], v[10:11], v[6:7]
	v_and_b32_e32 v11, 0xffff0000, v64
	v_and_b32_e32 v10, 0xffff0000, v63
	v_and_b32_e32 v63, 0xffff0000, v65
	v_and_b32_e32 v62, 0xffff0000, v62
	v_mov_b32_e32 v14, v9
	v_add_u32_e32 v64, s14, v105
	v_add_u32_e32 v65, s14, v106
	v_pk_mul_f32 v[14:15], v[14:15], v[62:63]
	v_add_u32_e32 v9, s18, v106
	v_add_u32_e32 v62, s18, v114
	v_add_u32_e32 v63, s18, v115
	v_add_u32_e32 v67, s14, v115
	ds_read_b32 v68, v8
	ds_read_b32 v78, v9
	ds_read_b32 v69, v62
	ds_read_b32 v80, v63
	ds_read_b32 v70, v64
	ds_read_b32 v79, v65
	ds_read_b32 v71, v66
	ds_read_b32 v81, v67
	v_pk_mul_f32 v[64:65], v[50:51], v[60:61]
	v_pk_mul_f32 v[60:61], v[48:49], v[60:61]
	v_mov_b32_e32 v4, v12
	v_mov_b32_e32 v5, v16
	v_mov_b32_e32 v12, v13
	v_mov_b32_e32 v13, v17
	v_pk_fma_f32 v[64:65], v[48:49], v[16:17], v[64:65] neg_lo:[0,0,1] neg_hi:[0,0,1]
	v_pk_fma_f32 v[16:17], v[50:51], v[16:17], v[60:61]
	s_waitcnt lgkmcnt(0)
	v_lshlrev_b32_e32 v8, 16, v68
	v_and_b32_e32 v9, 0xffff0000, v68
	s_waitcnt lgkmcnt(5)
	v_lshlrev_b32_e32 v62, 16, v69
	v_and_b32_e32 v63, 0xffff0000, v69
	v_pk_mul_f32 v[66:67], v[46:47], v[16:17]
	v_pk_mul_f32 v[68:69], v[50:51], v[16:17]
	v_pk_mul_f32 v[16:17], v[48:49], v[16:17]
	v_pk_mul_f32 v[60:61], v[66:67], v[62:63]
	v_pk_fma_f32 v[16:17], v[50:51], v[64:65], v[16:17]
	v_pk_fma_f32 v[60:61], v[64:65], v[8:9], v[60:61]
	s_waitcnt lgkmcnt(3)
	v_lshlrev_b32_e32 v8, 16, v70
	v_and_b32_e32 v9, 0xffff0000, v70
	s_waitcnt lgkmcnt(1)
	v_lshlrev_b32_e32 v62, 16, v71
	v_and_b32_e32 v63, 0xffff0000, v71
	v_pk_mul_f32 v[70:71], v[46:47], v[16:17]
	v_pk_fma_f32 v[68:69], v[48:49], v[64:65], v[68:69] neg_lo:[0,0,1] neg_hi:[0,0,1]
	v_pk_mul_f32 v[62:63], v[70:71], v[62:63]
	s_waitcnt lgkmcnt(0)
	v_lshlrev_b32_e32 v73, 16, v81
	v_lshlrev_b32_e32 v72, 16, v80
	v_mov_b32_e32 v76, v66
	v_mov_b32_e32 v77, v70
	v_pk_fma_f32 v[62:63], v[68:69], v[8:9], v[62:63]
	v_lshlrev_b32_e32 v9, 16, v79
	v_lshlrev_b32_e32 v8, 16, v78
	v_pk_mul_f32 v[72:73], v[76:77], v[72:73]
	v_and_b32_e32 v77, 0xffff0000, v79
	v_and_b32_e32 v76, 0xffff0000, v78
	v_and_b32_e32 v79, 0xffff0000, v81
	v_and_b32_e32 v78, 0xffff0000, v80
	v_mov_b32_e32 v70, v67
	v_mov_b32_e32 v74, v64
	v_pk_mul_f32 v[78:79], v[70:71], v[78:79]
	v_add_u32_e32 v64, s13, v105
	v_add_u32_e32 v70, s33, v105
	v_add_u32_e32 v71, s33, v106
	v_mov_b32_e32 v80, v65
	v_add_u32_e32 v65, s13, v106
	v_add_u32_e32 v66, s13, v114
	v_add_u32_e32 v67, s13, v115
	v_add_u32_e32 v82, s33, v114
	v_add_u32_e32 v83, s33, v115
	ds_read_b32 v84, v64
	ds_read_b32 v145, v65
	ds_read_b32 v85, v66
	ds_read_b32 v146, v67
	ds_read_b32 v86, v70
	ds_read_b32 v147, v71
	ds_read_b32 v87, v82
	ds_read_b32 v148, v83
	v_pk_mul_f32 v[70:71], v[50:51], v[16:17]
	v_pk_mul_f32 v[16:17], v[48:49], v[16:17]
	v_mov_b32_e32 v75, v68
	v_pk_fma_f32 v[16:17], v[50:51], v[68:69], v[16:17]
	v_mov_b32_e32 v81, v69
	s_waitcnt lgkmcnt(0)
	v_lshlrev_b32_e32 v64, 16, v84
	v_and_b32_e32 v65, 0xffff0000, v84
	s_waitcnt lgkmcnt(5)
	v_lshlrev_b32_e32 v66, 16, v85
	v_and_b32_e32 v67, 0xffff0000, v85
	v_pk_fma_f32 v[70:71], v[48:49], v[68:69], v[70:71] neg_lo:[0,0,1] neg_hi:[0,0,1]
	v_pk_mul_f32 v[68:69], v[46:47], v[16:17]
	v_pk_mul_f32 v[84:85], v[50:51], v[16:17]
	v_pk_mul_f32 v[16:17], v[48:49], v[16:17]
	v_pk_mul_f32 v[66:67], v[68:69], v[66:67]
	v_pk_fma_f32 v[16:17], v[50:51], v[70:71], v[16:17]
	v_pk_fma_f32 v[64:65], v[70:71], v[64:65], v[66:67]
	s_waitcnt lgkmcnt(3)
	v_lshlrev_b32_e32 v66, 16, v86
	v_and_b32_e32 v67, 0xffff0000, v86
	s_waitcnt lgkmcnt(1)
	v_lshlrev_b32_e32 v82, 16, v87
	v_and_b32_e32 v83, 0xffff0000, v87
	v_pk_mul_f32 v[86:87], v[46:47], v[16:17]
	v_pk_fma_f32 v[84:85], v[48:49], v[70:71], v[84:85] neg_lo:[0,0,1] neg_hi:[0,0,1]
	v_pk_mul_f32 v[82:83], v[86:87], v[82:83]
	s_waitcnt lgkmcnt(0)
	v_lshlrev_b32_e32 v89, 16, v148
	v_lshlrev_b32_e32 v88, 16, v146
	v_mov_b32_e32 v92, v68
	v_mov_b32_e32 v93, v86
	v_pk_fma_f32 v[66:67], v[84:85], v[66:67], v[82:83]
	v_lshlrev_b32_e32 v83, 16, v147
	v_pk_mul_f32 v[88:89], v[92:93], v[88:89]
	v_and_b32_e32 v93, 0xffff0000, v147
	v_and_b32_e32 v147, 0xffff0000, v148
	v_and_b32_e32 v146, 0xffff0000, v146
	v_mov_b32_e32 v86, v69
	v_lshlrev_b32_e32 v82, 16, v145
	v_and_b32_e32 v92, 0xffff0000, v145
	v_pk_mul_f32 v[86:87], v[86:87], v[146:147]
	v_add_u32_e32 v68, s25, v105
	v_add_u32_e32 v145, s10, v105
	v_add_u32_e32 v146, s10, v106
	v_add_u32_e32 v147, s10, v114
	v_mov_b32_e32 v90, v70
	v_mov_b32_e32 v148, v71
	v_add_u32_e32 v69, s25, v106
	v_add_u32_e32 v70, s25, v114
	v_add_u32_e32 v71, s25, v115
	v_add_u32_e32 v150, s10, v115
	ds_read_b32 v151, v68
	ds_read_b32 v152, v69
	ds_read_b32 v153, v70
	ds_read_b32 v154, v71
	ds_read_b32 v145, v145
	ds_read_b32 v155, v146
	ds_read_b32 v157, v147
	ds_read_b32 v160, v150
	v_pk_mul_f32 v[146:147], v[50:51], v[16:17]
	v_pk_mul_f32 v[16:17], v[48:49], v[16:17]
	v_mov_b32_e32 v91, v84
	v_pk_fma_f32 v[16:17], v[50:51], v[84:85], v[16:17]
	v_mov_b32_e32 v149, v85
	v_pk_fma_f32 v[146:147], v[48:49], v[84:85], v[146:147] neg_lo:[0,0,1] neg_hi:[0,0,1]
	v_pk_mul_f32 v[84:85], v[46:47], v[16:17]
	v_pk_mul_f32 v[158:159], v[50:51], v[16:17]
	v_pk_mul_f32 v[16:17], v[48:49], v[16:17]
	s_waitcnt lgkmcnt(0)
	s_cmpk_eq_i32 s4, 0x7c0
	s_cbranch_scc1 .Lmx_qk_skip_r
	v_add_u32_e32 v176, s4, v110
	v_add_u32_e32 v177, s24, v121
	v_add_u32_e32 v178, 64, v176
	v_add_u32_e32 v179, 0x7bf, v177
	v_cndmask_b32_e64 v178, v179, v178, s[76:77]
	v_add_u32_e32 v178, s84, v178
	v_mad_i64_i32 v[178:179], s[100:101], v178, s20, v[38:39]
	s_mov_b32 m0, s19
	v_lshl_add_u64 v[180:181], v[178:179], 0, s[80:81]
	global_load_lds_dwordx4 v[180:181], off
	v_lshl_add_u64 v[178:179], v[178:179], 0, s[6:7]
	s_mov_b32 m0, s82
	v_add_u32_e32 v176, 0x44, v176
	global_load_lds_dwordx4 v[178:179], off
	v_add_u32_e32 v178, 0x7bb, v177
	v_cndmask_b32_e64 v176, v178, v176, s[76:77]
	v_add_u32_e32 v176, s84, v176
	v_mad_i64_i32 v[178:179], s[100:101], v176, s20, v[38:39]
	v_lshl_add_u64 v[180:181], v[178:179], 0, s[80:81]
	s_mov_b32 m0, s85
	v_lshl_add_u64 v[178:179], v[178:179], 0, s[6:7]
	global_load_lds_dwordx4 v[180:181], off
	s_mov_b32 m0, s86
	s_nop 0
	global_load_lds_dwordx4 v[178:179], off
.Lmx_qk_skip_r:
	v_lshlrev_b32_e32 v70, 16, v153
	v_and_b32_e32 v71, 0xffff0000, v153
	v_pk_fma_f32 v[16:17], v[50:51], v[146:147], v[16:17]
	v_lshlrev_b32_e32 v68, 16, v151
	v_and_b32_e32 v69, 0xffff0000, v151
	v_lshlrev_b32_e32 v150, 16, v152
	v_and_b32_e32 v151, 0xffff0000, v152
	s_waitcnt lgkmcnt(4)
	v_lshlrev_b32_e32 v152, 16, v154
	v_pk_mul_f32 v[70:71], v[84:85], v[70:71]
	s_waitcnt lgkmcnt(1)
	v_lshlrev_b32_e32 v156, 16, v157
	v_and_b32_e32 v157, 0xffff0000, v157
	v_pk_mul_f32 v[16:17], v[46:47], v[16:17]
	v_pk_fma_f32 v[68:69], v[146:147], v[68:69], v[70:71]
	v_mul_f32_e32 v150, v146, v150
	v_mul_f32_e32 v84, v84, v152
	v_mul_f32_e32 v152, v147, v151
	v_lshlrev_b32_e32 v70, 16, v145
	v_and_b32_e32 v71, 0xffff0000, v145
	v_pk_fma_f32 v[158:159], v[48:49], v[146:147], v[158:159] neg_lo:[0,0,1] neg_hi:[0,0,1]
	v_pk_mul_f32 v[146:147], v[16:17], v[156:157]
	v_mov_b32_e32 v156, v158
	v_pk_fma_f32 v[70:71], v[158:159], v[70:71], v[146:147]
	s_waitcnt lgkmcnt(0)
	v_lshlrev_b32_e32 v147, 16, v160
	v_lshlrev_b32_e32 v146, 16, v155
	v_mov_b32_e32 v157, v16
	v_pk_fma_f32 v[2:3], v[4:5], v[2:3], v[6:7]
	v_pk_fma_f32 v[4:5], v[74:75], v[8:9], v[72:73]
	v_and_b32_e32 v73, 0xffff0000, v160
	v_and_b32_e32 v72, 0xffff0000, v155
	v_mov_b32_e32 v16, v159
	v_and_b32_e32 v153, 0xffff0000, v154
	v_pk_mul_f32 v[146:147], v[156:157], v[146:147]
	v_pk_mul_f32 v[16:17], v[16:17], v[72:73]
	v_mul_f32_e32 v154, v85, v153
	v_mov_b32_e32 v151, v146
	v_mov_b32_e32 v85, v147
	v_mov_b32_e32 v153, v16
	v_mov_b32_e32 v155, v17
	v_pk_fma_f32 v[6:7], v[90:91], v[82:83], v[88:89]
	v_pk_add_f32 v[8:9], v[150:151], v[84:85]
	v_pk_fma_f32 v[10:11], v[12:13], v[10:11], v[14:15]
	v_pk_fma_f32 v[12:13], v[80:81], v[76:77], v[78:79]
	v_pk_fma_f32 v[14:15], v[148:149], v[92:93], v[86:87]
	v_pk_add_f32 v[16:17], v[152:153], v[154:155]
	v_mov_b32_e32 v88, 0
	v_pk_mul_f32 v[8:9], v[8:9], s[34:35] op_sel_hi:[1,0]
	v_pk_mul_f32 v[6:7], v[6:7], s[34:35] op_sel_hi:[1,0]
	v_pk_mul_f32 v[4:5], v[4:5], s[34:35] op_sel_hi:[1,0]
	v_pk_mul_f32 v[2:3], v[2:3], s[34:35] op_sel_hi:[1,0]
	v_pk_mul_f32 v[16:17], v[16:17], s[34:35] op_sel_hi:[1,0]
	v_pk_mul_f32 v[14:15], v[14:15], s[34:35] op_sel_hi:[1,0]
	v_pk_mul_f32 v[12:13], v[12:13], s[34:35] op_sel_hi:[1,0]
	v_pk_mul_f32 v[10:11], v[10:11], s[34:35] op_sel_hi:[1,0]
	v_mov_b32_e32 v86, 0
	v_mov_b32_e32 v84, 0
	v_mov_b32_e32 v82, 0
	v_mov_b32_e32 v78, 0
	v_mov_b32_e32 v80, 0
	v_mov_b32_e32 v73, 0
	v_mov_b32_e32 v157, 0
	v_mov_b32_e32 v156, 0
	v_mov_b32_e32 v155, 0
	v_mov_b32_e32 v154, 0
	v_mov_b32_e32 v92, 0
	v_mov_b32_e32 v90, 0
	v_mov_b32_e32 v76, 0
	v_mov_b32_e32 v158, 0
	v_mov_b32_e32 v77, v88
.LBB0_470:
	v_add_u32_e32 v72, s16, v102
	v_add_u32_e32 v74, s0, v102
	ds_read_u16 v145, v72
	ds_read_u16 v149, v72 offset:128
	ds_read_u16 v146, v72 offset:256
	ds_read_u16 v150, v72 offset:384
	ds_read_u16 v147, v74
	ds_read_u16 v151, v72 offset:640
	ds_read_u16 v148, v72 offset:768
	ds_read_u16 v152, v72 offset:896
	v_add_u32_e32 v72, s17, v103
	ds_write_b64 v72, v[76:77]
	s_waitcnt lgkmcnt(0)
	s_cmpk_eq_i32 s4, 0x7c0
	s_cbranch_scc1 .Lmx_v_skip
	v_add_u32_e32 v176, s4, v119
	v_add_u32_e32 v177, s24, v120
	v_cndmask_b32_e64 v176, v177, v176, s[76:77]
	v_add_u32_e32 v176, s84, v176
	v_mad_i64_i32 v[178:179], s[100:101], v176, s20, v[52:53]
	s_mov_b32 m0, s87
	s_nop 0
	global_load_lds_dwordx4 v[178:179], off
.Lmx_v_skip:
	s_barrier
.LBB0_472:
	s_mov_b64 s[8:9], -1
	s_and_b64 vcc, exec, s[78:79]
	v_add_u32_e32 v72, 0, v103
	v_add_u32_e32 v153, s1, v108
	s_cbranch_vccnz .LBB0_474
	v_add_u32_e32 v74, 0x1a000, v72
	ds_read2st64_b64 v[160:163], v74 offset1:1
	ds_read2st64_b64 v[164:167], v74 offset0:2 offset1:3
	ds_read2st64_b64 v[168:171], v74 offset0:4 offset1:5
	ds_read2st64_b64 v[172:175], v74 offset0:6 offset1:7
	s_mov_b64 s[8:9], 0
	s_waitcnt lgkmcnt(0)
	v_pk_add_f32 v[74:75], v[160:161], 0 op_sel_hi:[1,0]
	s_nop 0
	v_cndmask_b32_e64 v81, 0, v74, s[60:61]
	v_cndmask_b32_e64 v79, 0, v75, s[60:61]
	v_add_f32_e32 v83, v162, v81
	v_add_f32_e32 v85, v163, v79
	v_cndmask_b32_e64 v81, v81, v83, s[62:63]
	v_cndmask_b32_e64 v79, v79, v85, s[62:63]
	v_add_f32_e32 v83, v164, v81
	v_add_f32_e32 v85, v165, v79
	v_cndmask_b32_e64 v81, v81, v83, s[64:65]
	v_pk_add_f32 v[74:75], v[74:75], v[162:163]
	v_cndmask_b32_e64 v79, v79, v85, s[64:65]
	v_add_f32_e32 v83, v166, v81
	v_pk_add_f32 v[74:75], v[74:75], v[164:165]
	v_add_f32_e32 v85, v167, v79
	v_cndmask_b32_e64 v81, v81, v83, s[66:67]
	v_cndmask_b32_e64 v79, v79, v85, s[66:67]
	v_pk_add_f32 v[160:161], v[74:75], v[166:167]
	v_add_f32_e32 v74, v168, v81
	v_add_f32_e32 v75, v169, v79
	v_cndmask_b32_e64 v81, v81, v74, s[68:69]
	v_cndmask_b32_e64 v79, v79, v75, s[68:69]
	v_add_f32_e32 v83, v170, v81
	v_add_f32_e32 v85, v171, v79
	v_cndmask_b32_e64 v81, v81, v83, s[70:71]
	v_cndmask_b32_e64 v79, v79, v85, s[70:71]
	v_add_f32_e32 v83, v172, v81
	v_add_f32_e32 v85, v173, v79
	v_cndmask_b32_e64 v81, v81, v83, s[72:73]
	v_cndmask_b32_e64 v79, v79, v85, s[72:73]
	v_add_f32_e32 v83, v174, v81
	v_add_f32_e32 v85, v175, v79
	v_cndmask_b32_e64 v159, v81, v83, s[74:75]
	v_cndmask_b32_e64 v91, v79, v85, s[74:75]
	v_add_f32_e32 v79, v158, v159
	v_sub_f32_e32 v79, v79, v160
	v_add_f32_e32 v81, v88, v91
	v_med3_f32 v79, v79, s12, v228
	v_exp_f32_e32 v88, v79
	v_sub_f32_e32 v79, v81, v161
	v_med3_f32 v79, v79, s12, v228
	v_exp_f32_e32 v89, v79
	v_add_f32_e32 v81, v157, v159
	v_sub_f32_e32 v81, v81, v160
	v_add_f32_e32 v83, v86, v91
	v_med3_f32 v81, v81, s12, v228
	v_exp_f32_e32 v86, v81
	v_sub_f32_e32 v81, v83, v161
	v_rcp_f32_e32 v164, v88
	v_rcp_f32_e32 v165, v89
	v_med3_f32 v81, v81, s12, v228
	v_exp_f32_e32 v87, v81
	v_pk_mul_f32 v[88:89], v[56:57], v[88:89]
	v_add_f32_e32 v85, v84, v91
	v_cvt_pk_bf16_f32 v79, v88, v89
	v_mov_b32_e32 v88, v2
	v_mov_b32_e32 v89, v10
	v_pk_mul_f32 v[88:89], v[88:89], v[164:165]
	v_add_f32_e32 v73, v73, v91
	v_cvt_pk_bf16_f32 v81, v88, v89
	v_rcp_f32_e32 v88, v86
	v_rcp_f32_e32 v89, v87
	v_pk_mul_f32 v[86:87], v[58:59], v[86:87]
	v_add_f32_e32 v76, v76, v159
	v_cvt_pk_bf16_f32 v83, v86, v87
	ds_write2_b32 v153, v79, v83 offset1:68
	v_add_f32_e32 v83, v156, v159
	v_sub_f32_e32 v83, v83, v160
	v_mov_b32_e32 v86, v3
	v_mov_b32_e32 v87, v11
	v_med3_f32 v83, v83, s12, v228
	v_pk_mul_f32 v[86:87], v[86:87], v[88:89]
	v_exp_f32_e32 v84, v83
	v_sub_f32_e32 v83, v85, v161
	v_cvt_pk_bf16_f32 v79, v86, v87
	v_med3_f32 v83, v83, s12, v228
	v_add_u32_e32 v86, 0x4400, v153
	v_exp_f32_e32 v85, v83
	ds_write2_b32 v86, v81, v79 offset1:68
	v_add_f32_e32 v81, v155, v159
	v_sub_f32_e32 v81, v81, v160
	v_add_f32_e32 v83, v82, v91
	v_med3_f32 v81, v81, s12, v228
	v_exp_f32_e32 v82, v81
	v_sub_f32_e32 v81, v83, v161
	v_rcp_f32_e32 v156, v84
	v_rcp_f32_e32 v157, v85
	v_med3_f32 v81, v81, s12, v228
	v_exp_f32_e32 v83, v81
	v_pk_mul_f32 v[84:85], v[60:61], v[84:85]
	v_add_f32_e32 v87, v78, v91
	v_cvt_pk_bf16_f32 v79, v84, v85
	v_mov_b32_e32 v84, v4
	v_mov_b32_e32 v85, v12
	v_pk_mul_f32 v[84:85], v[84:85], v[156:157]
	v_add_f32_e32 v77, v77, v91
	v_cvt_pk_bf16_f32 v81, v84, v85
	v_rcp_f32_e32 v84, v82
	v_rcp_f32_e32 v85, v83
	v_pk_mul_f32 v[82:83], v[62:63], v[82:83]
	v_sub_f32_e32 v73, v73, v161
	v_cvt_pk_bf16_f32 v82, v82, v83
	ds_write2_b32 v153, v79, v82 offset0:136 offset1:204
	v_add_f32_e32 v79, v154, v159
	v_mov_b32_e32 v82, v5
	v_mov_b32_e32 v83, v13
	v_sub_f32_e32 v78, v79, v160
	v_sub_f32_e32 v79, v87, v161
	v_pk_mul_f32 v[82:83], v[82:83], v[84:85]
	v_med3_f32 v78, v78, s12, v228
	v_med3_f32 v79, v79, s12, v228
	v_exp_f32_e32 v78, v78
	v_exp_f32_e32 v79, v79
	v_cvt_pk_bf16_f32 v82, v82, v83
	ds_write2_b32 v86, v81, v82 offset0:136 offset1:204
	v_add_f32_e32 v81, v92, v159
	v_add_f32_e32 v83, v80, v91
	v_sub_f32_e32 v80, v81, v160
	v_sub_f32_e32 v81, v83, v161
	v_med3_f32 v80, v80, s12, v228
	v_med3_f32 v81, v81, s12, v228
	v_rcp_f32_e32 v154, v78
	v_rcp_f32_e32 v155, v79
	v_exp_f32_e32 v80, v80
	v_exp_f32_e32 v81, v81
	v_pk_mul_f32 v[78:79], v[64:65], v[78:79]
	v_add_u32_e32 v86, 0x400, v153
	v_cvt_pk_bf16_f32 v82, v78, v79
	v_mov_b32_e32 v78, v6
	v_mov_b32_e32 v79, v14
	v_pk_mul_f32 v[78:79], v[78:79], v[154:155]
	v_rcp_f32_e32 v92, v80
	v_rcp_f32_e32 v93, v81
	v_cvt_pk_bf16_f32 v83, v78, v79
	v_pk_mul_f32 v[78:79], v[66:67], v[80:81]
	v_sub_f32_e32 v76, v76, v160
	v_cvt_pk_bf16_f32 v78, v78, v79
	ds_write2_b32 v86, v82, v78 offset0:16 offset1:84
	v_mov_b32_e32 v78, v7
	v_mov_b32_e32 v79, v15
	v_pk_mul_f32 v[78:79], v[78:79], v[92:93]
	v_sub_f32_e32 v77, v77, v161
	v_cvt_pk_bf16_f32 v80, v78, v79
	v_add_f32_e32 v78, v90, v159
	v_sub_f32_e32 v78, v78, v160
	v_med3_f32 v78, v78, s12, v228
	v_med3_f32 v73, v73, s12, v228
	v_med3_f32 v76, v76, s12, v228
	v_med3_f32 v77, v77, s12, v228
	v_pk_add_f32 v[74:75], v[160:161], v[168:169]
	v_exp_f32_e32 v78, v78
	v_exp_f32_e32 v79, v73
	v_exp_f32_e32 v76, v76
	v_exp_f32_e32 v77, v77
	v_pk_add_f32 v[74:75], v[74:75], v[170:171]
	v_add_u32_e32 v73, 0x4800, v153
	v_pk_add_f32 v[74:75], v[74:75], v[172:173]
	ds_write2_b32 v73, v83, v80 offset0:16 offset1:84
	v_pk_add_f32 v[74:75], v[74:75], v[174:175]
	v_rcp_f32_e32 v80, v78
	v_pk_add_f32 v[162:163], v[74:75], v[160:161] neg_lo:[0,1] neg_hi:[0,1]
	v_rcp_f32_e32 v81, v79
	v_rcp_f32_e32 v160, v76
	v_rcp_f32_e32 v161, v77
	v_pk_mul_f32 v[78:79], v[68:69], v[78:79]
	v_pk_mul_f32 v[76:77], v[70:71], v[76:77]
	v_cvt_pk_bf16_f32 v82, v78, v79
	v_cvt_pk_bf16_f32 v76, v76, v77
	v_exp_f32_e32 v158, v162
	v_mov_b32_e32 v78, v8
	v_mov_b32_e32 v79, v16
	ds_write2_b32 v86, v82, v76 offset0:152 offset1:220
	v_mov_b32_e32 v76, v9
	v_mov_b32_e32 v77, v17
	v_exp_f32_e32 v162, v163
	v_pk_mul_f32 v[78:79], v[78:79], v[80:81]
	v_pk_mul_f32 v[76:77], v[76:77], v[160:161]
	v_cvt_pk_bf16_f32 v78, v78, v79
	v_cvt_pk_bf16_f32 v76, v76, v77
	ds_write2_b32 v73, v78, v76 offset0:152 offset1:220
	v_mov_b32_e32 v76, v164
	v_mov_b32_e32 v77, v88
	v_mov_b32_e32 v78, v156
	v_mov_b32_e32 v79, v84
	v_mov_b32_e32 v82, v154
	v_mov_b32_e32 v83, v92
	v_mov_b32_e32 v86, v80
	v_mov_b32_e32 v87, v160
	v_pk_mul_f32 v[76:77], v[158:159], v[76:77] op_sel_hi:[0,1]
	v_pk_mul_f32 v[78:79], v[158:159], v[78:79] op_sel_hi:[0,1]
	v_pk_mul_f32 v[82:83], v[158:159], v[82:83] op_sel_hi:[0,1]
	v_pk_mul_f32 v[86:87], v[158:159], v[86:87] op_sel_hi:[0,1]
	v_mov_b32_e32 v88, v165
	v_mov_b32_e32 v84, v157
	v_mov_b32_e32 v92, v155
	v_mov_b32_e32 v160, v81
	v_pk_mul_f32 v[90:91], v[8:9], v[86:87]
	v_pk_mul_f32 v[86:87], v[6:7], v[82:83]
	v_pk_mul_f32 v[82:83], v[4:5], v[78:79]
	v_pk_mul_f32 v[78:79], v[2:3], v[76:77]
	v_pk_mul_f32 v[76:77], v[162:163], v[88:89] op_sel_hi:[0,1]
	v_pk_mul_f32 v[84:85], v[162:163], v[84:85] op_sel_hi:[0,1]
	v_pk_mul_f32 v[88:89], v[162:163], v[92:93] op_sel_hi:[0,1]
	v_pk_mul_f32 v[80:81], v[162:163], v[160:161] op_sel_hi:[0,1]
	v_pk_mul_f32 v[92:93], v[16:17], v[80:81]
	v_pk_mul_f32 v[88:89], v[14:15], v[88:89]
	v_pk_mul_f32 v[84:85], v[12:13], v[84:85]
	v_pk_mul_f32 v[80:81], v[10:11], v[76:77]

.LBB0_991:
	s_add_i32 s4, s8, 7
	s_ashr_i32 s4, s4, 3
	s_add_i32 s100, s4, 31
	s_lshr_b32 s100, s100, 5
	s_max_u32 s100, s100, 1
	s_add_i32 s101, s4, s100
	s_add_i32 s101, s101, -1
	s_mov_b32 s7, 0
.Lnxa8_loop:
	s_cmp_lt_u32 s101, s100
	s_cbranch_scc1 .Lnxa8_done
	s_sub_i32 s101, s101, s100
	s_add_i32 s7, s7, 1
	s_branch .Lnxa8_loop
.Lnxa8_done:
	v_readlane_b32 s5, v254, 29
	s_mul_i32 s5, s4, s5
	v_readlane_b32 s6, v254, 30
	s_add_i32 s10, s5, s6
	s_cmp_lt_i32 s6, s7
	s_cselect_b64 s[4:5], -1, 0
	s_cmp_lt_i32 s10, s8
	s_cselect_b64 s[6:7], -1, 0
	s_and_b64 s[4:5], s[4:5], s[6:7]

.LBB0_999:
	s_add_i32 s6, s16, 7
	s_ashr_i32 s6, s6, 3
	s_add_i32 s100, s6, 31
	s_lshr_b32 s100, s100, 5
	s_max_u32 s100, s100, 1
	s_add_i32 s101, s6, s100
	s_add_i32 s101, s101, -1
	s_mov_b32 s9, 0
.Lnxb8_loop:
	s_cmp_lt_u32 s101, s100
	s_cbranch_scc1 .Lnxb8_done
	s_sub_i32 s101, s101, s100
	s_add_i32 s9, s9, 1
	s_branch .Lnxb8_loop
.Lnxb8_done:
	v_readlane_b32 s8, v254, 30
	s_cmp_lt_i32 s8, s9
	s_cselect_b32 s100, 0, 0x10000
	s_mul_i32 s7, s71, s9
	s_add_i32 s7, s7, s8
	s_add_i32 s7, s7, s100
	v_readlane_b32 s8, v254, 29
	s_mul_i32 s8, s6, s8
	s_add_i32 s14, s8, s7
	s_cmp_lt_i32 s7, s6
	s_cselect_b64 s[6:7], -1, 0
	s_cmp_lt_i32 s14, s16
	s_cselect_b64 s[8:9], -1, 0
	s_and_b64 s[8:9], s[6:7], s[8:9]

.LBB0_1182:
	v_readfirstlane_b32 s100, v3
	s_add_i32 s101, s100, 31
	s_lshr_b32 s101, s101, 5
	s_max_u32 s101, s101, 1
	s_add_i32 s40, s100, s101
	s_add_i32 s40, s40, -1
	s_mov_b32 s41, 0
.Lnxa9_loop:
	s_cmp_lt_u32 s40, s101
	s_cbranch_scc1 .Lnxa9_done
	s_sub_i32 s40, s40, s101
	s_add_i32 s41, s41, 1
	s_branch .Lnxa9_loop
.Lnxa9_done:
	v_readlane_b32 s6, v254, 29
	s_nop 1
	v_mul_lo_u32 v2, v3, s6
	v_readlane_b32 s6, v254, 30
	s_nop 1
	v_add_u32_e32 v2, s6, v2
	s_cmp_lt_i32 s6, s41
	s_cselect_b64 s[100:101], -1, 0
	v_cmp_lt_i32_e64 s[40:41], v2, v4
	s_and_b64 s[6:7], s[100:101], s[40:41]

.LBB0_1189:
	v_readfirstlane_b32 s100, v2
	s_add_i32 s101, s100, 31
	s_lshr_b32 s101, s101, 5
	s_max_u32 s101, s101, 1
	s_add_i32 s40, s100, s101
	s_add_i32 s40, s40, -1
	s_mov_b32 s41, 0

.Lnxb9_done:
	v_readlane_b32 s9, v254, 30
	s_cmp_lt_i32 s9, s41
	s_cselect_b32 s40, 0, 0x10000
	s_mul_i32 s8, s54, s41
	s_add_i32 s8, s8, s9
	s_add_i32 s8, s8, s40
	v_readlane_b32 s9, v254, 29
	v_cmp_lt_i32_e32 vcc, s8, v2
	s_nop 0
	v_mul_lo_u32 v4, v2, s9
	v_add_u32_e32 v6, s8, v4
	v_cmp_lt_i32_e64 s[40:41], v6, v3
	s_and_b64 s[38:39], vcc, s[40:41]

	.amdhsa_kernel _Z4mega6Params
		.amdhsa_group_segment_fixed_size 0
		.amdhsa_private_segment_fixed_size 0
		.amdhsa_kernarg_size 440
		.amdhsa_user_sgpr_count 2
		.amdhsa_user_sgpr_dispatch_ptr 0
		.amdhsa_user_sgpr_queue_ptr 0
		.amdhsa_user_sgpr_kernarg_segment_ptr 1
		.amdhsa_user_sgpr_dispatch_id 0
		.amdhsa_user_sgpr_kernarg_preload_length 0
		.amdhsa_user_sgpr_kernarg_preload_offset 0
		.amdhsa_user_sgpr_private_segment_size 0
		.amdhsa_uses_dynamic_stack 0
		.amdhsa_enable_private_segment 0
		.amdhsa_system_sgpr_workgroup_id_x 1
		.amdhsa_system_sgpr_workgroup_id_y 0
		.amdhsa_system_sgpr_workgroup_id_z 0
		.amdhsa_system_sgpr_workgroup_info 0
		.amdhsa_system_vgpr_workitem_id 0
		.amdhsa_next_free_vgpr 256
		.amdhsa_next_free_sgpr 102
		.amdhsa_accum_offset 256
		.amdhsa_reserve_vcc 1
		.amdhsa_float_round_mode_32 0
		.amdhsa_float_round_mode_16_64 0
		.amdhsa_float_denorm_mode_32 3
		.amdhsa_float_denorm_mode_16_64 3
		.amdhsa_dx10_clamp 1
		.amdhsa_ieee_mode 1
		.amdhsa_fp16_overflow 0
		.amdhsa_tg_split 0
		.amdhsa_exception_fp_ieee_invalid_op 0
		.amdhsa_exception_fp_denorm_src 0
		.amdhsa_exception_fp_ieee_div_zero 0
		.amdhsa_exception_fp_ieee_overflow 0
		.amdhsa_exception_fp_ieee_underflow 0
		.amdhsa_exception_fp_ieee_inexact 0
		.amdhsa_exception_int_div_zero 0
	.end_amdhsa_kernel

amdhsa.kernels:
  - .agpr_count:     0
    .args:
      - .offset:         0
        .size:           184
        .value_kind:     by_value
      - .offset:         184
        .size:           4
        .value_kind:     hidden_block_count_x
      - .offset:         188
        .size:           4
        .value_kind:     hidden_block_count_y
      - .offset:         192
        .size:           4
        .value_kind:     hidden_block_count_z
      - .offset:         196
        .size:           2
        .value_kind:     hidden_group_size_x
      - .offset:         198
        .size:           2
        .value_kind:     hidden_group_size_y
      - .offset:         200
        .size:           2
        .value_kind:     hidden_group_size_z
      - .offset:         202
        .size:           2
        .value_kind:     hidden_remainder_x
      - .offset:         204
        .size:           2
        .value_kind:     hidden_remainder_y
      - .offset:         206
        .size:           2
        .value_kind:     hidden_remainder_z
      - .offset:         224
        .size:           8
        .value_kind:     hidden_global_offset_x
      - .offset:         232
        .size:           8
        .value_kind:     hidden_global_offset_y
      - .offset:         240
        .size:           8
        .value_kind:     hidden_global_offset_z
      - .offset:         248
        .size:           2
        .value_kind:     hidden_grid_dims
      - .offset:         304
        .size:           4
        .value_kind:     hidden_dynamic_lds_size
    .group_segment_fixed_size: 0
    .kernarg_segment_align: 8
    .kernarg_segment_size: 440
    .language:       OpenCL C
    .language_version:
      - 2
      - 0
    .max_flat_workgroup_size: 512
    .name:           _Z4mega6Params
    .private_segment_fixed_size: 0
    .sgpr_count:     108
    .sgpr_spill_count: 176
    .symbol:         _Z4mega6Params.kd
    .uniform_work_group_size: 1
    .uses_dynamic_stack: false
    .vgpr_count:     256
    .vgpr_spill_count: 0
    .wavefront_size: 64
